# speedup vs baseline: 1.0221x; 1.0221x over previous
_Z7xform_xPKfP15HIP_vector_typeIjLj4EE:
	s_load_dwordx4 s[4:7], s[0:1], 0x0
	s_lshr_b32 s8, s2, 2
	s_and_b32 s9, s2, 3
	v_and_b32_e32 v1, 15, v0
	v_lshrrev_b32_e32 v2, 4, v0
	v_lshrrev_b32_e32 v3, 3, v2
	v_and_b32_e32 v4, 7, v2
	s_lshl_b32 s10, s9, 3
	v_add_u32_e32 v5, s10, v4
	v_lshlrev_b32_e32 v5, 14, v5
	v_lshl_add_u32 v5, v3, 19, v5
	v_lshl_add_u32 v5, v1, 4, v5
	s_lshl_b32 s11, s8, 8
	v_add_u32_e32 v5, s11, v5
	v_xor_b32_e32 v40, v1, v3
	v_lshlrev_b32_e32 v42, 8, v2
	s_waitcnt lgkmcnt(0)
	s_mov_b32 s12, s4
	s_and_b32 s13, s5, 0xffff
	s_mov_b32 s14, 0x800000
	s_mov_b32 s15, 0x20000
	s_mov_b32 s16, s6
	s_and_b32 s17, s7, 0xffff
	s_mov_b32 s18, 0x400000
	s_mov_b32 s19, 0x20000
	s_mov_b32 s20, 0x0
	s_mov_b32 s21, 0x100000
	s_mov_b32 s22, 0x200000
	s_mov_b32 s23, 0x300000
	s_mov_b32 s24, 0x400000
	s_mov_b32 s25, 0x500000
	s_mov_b32 s26, 0x600000
	s_mov_b32 s27, 0x700000
	buffer_load_dwordx4 v[8:11], v5, s[12:15], s20 offen nt
	buffer_load_dwordx4 v[12:15], v5, s[12:15], s21 offen nt
	buffer_load_dwordx4 v[16:19], v5, s[12:15], s22 offen nt
	buffer_load_dwordx4 v[20:23], v5, s[12:15], s23 offen nt
	buffer_load_dwordx4 v[24:27], v5, s[12:15], s24 offen nt
	buffer_load_dwordx4 v[28:31], v5, s[12:15], s25 offen nt
	buffer_load_dwordx4 v[32:35], v5, s[12:15], s26 offen nt
	buffer_load_dwordx4 v[36:39], v5, s[12:15], s27 offen nt
	v_lshrrev_b32_e32 v43, 6, v0
	v_bfe_u32 v44, v0, 4, 2
	v_and_b32_e32 v45, 3, v1
	v_xor_b32_e32 v45, v43, v45
	v_lshlrev_b32_e32 v45, 4, v45
	v_lshl_add_u32 v45, v1, 11, v45
	v_lshl_add_u32 v45, v44, 2, v45
	v_lshrrev_b32_e32 v46, 2, v1
	s_lshl_b32 s28, s8, 16
	s_lshl_b32 s29, s9, 8
	s_add_u32 s28, s28, s29
	v_lshlrev_b32_e32 v48, 10, v2
	v_lshl_add_u32 v48, v1, 4, v48
	v_add_u32_e32 v48, s28, v48
	s_waitcnt vmcnt(7)
	v_xor_b32_e32 v41, 0, v40
	v_lshl_add_u32 v41, v41, 4, v42
	ds_write_b128 v41, v[8:11] offset:0
	s_waitcnt vmcnt(6)
	v_xor_b32_e32 v41, 2, v40
	v_lshl_add_u32 v41, v41, 4, v42
	ds_write_b128 v41, v[12:15] offset:4096
	s_waitcnt vmcnt(5)
	v_xor_b32_e32 v41, 4, v40
	v_lshl_add_u32 v41, v41, 4, v42
	ds_write_b128 v41, v[16:19] offset:8192
	s_waitcnt vmcnt(4)
	v_xor_b32_e32 v41, 6, v40
	v_lshl_add_u32 v41, v41, 4, v42
	ds_write_b128 v41, v[20:23] offset:12288
	s_waitcnt vmcnt(3)
	v_xor_b32_e32 v41, 8, v40
	v_lshl_add_u32 v41, v41, 4, v42
	ds_write_b128 v41, v[24:27] offset:16384
	s_waitcnt vmcnt(2)
	v_xor_b32_e32 v41, 10, v40
	v_lshl_add_u32 v41, v41, 4, v42
	ds_write_b128 v41, v[28:31] offset:20480
	s_waitcnt vmcnt(1)
	v_xor_b32_e32 v41, 12, v40
	v_lshl_add_u32 v41, v41, 4, v42
	ds_write_b128 v41, v[32:35] offset:24576
	s_waitcnt vmcnt(0)
	v_xor_b32_e32 v41, 14, v40
	v_lshl_add_u32 v41, v41, 4, v42
	ds_write_b128 v41, v[36:39] offset:28672
	s_waitcnt lgkmcnt(0)
	s_barrier
	v_xor_b32_e32 v47, 0, v46
	v_lshl_add_u32 v47, v47, 6, v45
	ds_read2st64_b32 v[50:51], v47 offset0:0 offset1:1
	ds_read2st64_b32 v[52:53], v47 offset0:2 offset1:3
	ds_read2st64_b32 v[54:55], v47 offset0:4 offset1:5
	ds_read2st64_b32 v[56:57], v47 offset0:6 offset1:7
	s_waitcnt lgkmcnt(3)
	v_cvt_pk_f16_f32 v60, v50, v51
	s_waitcnt lgkmcnt(2)
	v_cvt_pk_f16_f32 v61, v52, v53
	s_waitcnt lgkmcnt(1)
	v_cvt_pk_f16_f32 v62, v54, v55
	s_waitcnt lgkmcnt(0)
	v_cvt_pk_f16_f32 v63, v56, v57
	s_mov_b32 s30, 0x0
	buffer_store_dwordx4 v[60:63], v48, s[16:19], s30 offen
	v_xor_b32_e32 v47, 1, v46
	v_lshl_add_u32 v47, v47, 6, v45
	ds_read2st64_b32 v[50:51], v47 offset0:0 offset1:1
	ds_read2st64_b32 v[52:53], v47 offset0:2 offset1:3
	ds_read2st64_b32 v[54:55], v47 offset0:4 offset1:5
	ds_read2st64_b32 v[56:57], v47 offset0:6 offset1:7
	s_waitcnt lgkmcnt(3)
	v_cvt_pk_f16_f32 v64, v50, v51
	s_waitcnt lgkmcnt(2)
	v_cvt_pk_f16_f32 v65, v52, v53
	s_waitcnt lgkmcnt(1)
	v_cvt_pk_f16_f32 v66, v54, v55
	s_waitcnt lgkmcnt(0)
	v_cvt_pk_f16_f32 v67, v56, v57
	s_mov_b32 s30, 0x4000
	buffer_store_dwordx4 v[64:67], v48, s[16:19], s30 offen
	v_xor_b32_e32 v47, 2, v46
	v_lshl_add_u32 v47, v47, 6, v45
	ds_read2st64_b32 v[50:51], v47 offset0:0 offset1:1
	ds_read2st64_b32 v[52:53], v47 offset0:2 offset1:3
	ds_read2st64_b32 v[54:55], v47 offset0:4 offset1:5
	ds_read2st64_b32 v[56:57], v47 offset0:6 offset1:7
	s_waitcnt lgkmcnt(3)
	v_cvt_pk_f16_f32 v68, v50, v51
	s_waitcnt lgkmcnt(2)
	v_cvt_pk_f16_f32 v69, v52, v53
	s_waitcnt lgkmcnt(1)
	v_cvt_pk_f16_f32 v70, v54, v55
	s_waitcnt lgkmcnt(0)
	v_cvt_pk_f16_f32 v71, v56, v57
	s_mov_b32 s30, 0x8000
	buffer_store_dwordx4 v[68:71], v48, s[16:19], s30 offen
	v_xor_b32_e32 v47, 3, v46
	v_lshl_add_u32 v47, v47, 6, v45
	ds_read2st64_b32 v[50:51], v47 offset0:0 offset1:1
	ds_read2st64_b32 v[52:53], v47 offset0:2 offset1:3
	ds_read2st64_b32 v[54:55], v47 offset0:4 offset1:5
	ds_read2st64_b32 v[56:57], v47 offset0:6 offset1:7
	s_waitcnt lgkmcnt(3)
	v_cvt_pk_f16_f32 v72, v50, v51
	s_waitcnt lgkmcnt(2)
	v_cvt_pk_f16_f32 v73, v52, v53
	s_waitcnt lgkmcnt(1)
	v_cvt_pk_f16_f32 v74, v54, v55
	s_waitcnt lgkmcnt(0)
	v_cvt_pk_f16_f32 v75, v56, v57
	s_mov_b32 s30, 0xc000
	buffer_store_dwordx4 v[72:75], v48, s[16:19], s30 offen
	s_endpgm

	.amdhsa_kernel _Z7xform_xPKfP15HIP_vector_typeIjLj4EE
		.amdhsa_group_segment_fixed_size 34816
		.amdhsa_private_segment_fixed_size 0
		.amdhsa_kernarg_size 16
		.amdhsa_user_sgpr_count 2
		.amdhsa_user_sgpr_dispatch_ptr 0
		.amdhsa_user_sgpr_queue_ptr 0
		.amdhsa_user_sgpr_kernarg_segment_ptr 1
		.amdhsa_user_sgpr_dispatch_id 0
		.amdhsa_user_sgpr_kernarg_preload_length 0
		.amdhsa_user_sgpr_kernarg_preload_offset 0
		.amdhsa_user_sgpr_private_segment_size 0
		.amdhsa_uses_dynamic_stack 0
		.amdhsa_enable_private_segment 0
		.amdhsa_system_sgpr_workgroup_id_x 1
		.amdhsa_system_sgpr_workgroup_id_y 0
		.amdhsa_system_sgpr_workgroup_id_z 0
		.amdhsa_system_sgpr_workgroup_info 0
		.amdhsa_system_vgpr_workitem_id 0
		.amdhsa_next_free_vgpr 97
		.amdhsa_next_free_sgpr 96
		.amdhsa_accum_offset 76
		.amdhsa_reserve_vcc 0
		.amdhsa_float_round_mode_32 0
		.amdhsa_float_round_mode_16_64 0
		.amdhsa_float_denorm_mode_32 3
		.amdhsa_float_denorm_mode_16_64 3
		.amdhsa_dx10_clamp 1
		.amdhsa_ieee_mode 1
		.amdhsa_fp16_overflow 0
		.amdhsa_tg_split 0
		.amdhsa_exception_fp_ieee_invalid_op 0
		.amdhsa_exception_fp_denorm_src 0
		.amdhsa_exception_fp_ieee_div_zero 0
		.amdhsa_exception_fp_ieee_overflow 0
		.amdhsa_exception_fp_ieee_underflow 0
		.amdhsa_exception_fp_ieee_inexact 0
		.amdhsa_exception_int_div_zero 0
	.end_amdhsa_kernel

.Lfunc_end0:
	.size	_Z7xform_xPKfP15HIP_vector_typeIjLj4EE, .Lfunc_end0-_Z7xform_xPKfP15HIP_vector_typeIjLj4EE
	.set _Z7xform_xPKfP15HIP_vector_typeIjLj4EE.num_vgpr, 76
	.set _Z7xform_xPKfP15HIP_vector_typeIjLj4EE.num_agpr, 0
	.set _Z7xform_xPKfP15HIP_vector_typeIjLj4EE.numbered_sgpr, 31
	.set _Z7xform_xPKfP15HIP_vector_typeIjLj4EE.num_named_barrier, 0
	.set _Z7xform_xPKfP15HIP_vector_typeIjLj4EE.private_seg_size, 0
	.set _Z7xform_xPKfP15HIP_vector_typeIjLj4EE.uses_vcc, 0
	.set _Z7xform_xPKfP15HIP_vector_typeIjLj4EE.uses_flat_scratch, 0
	.set _Z7xform_xPKfP15HIP_vector_typeIjLj4EE.has_dyn_sized_stack, 0
	.set _Z7xform_xPKfP15HIP_vector_typeIjLj4EE.has_recursion, 0
	.set _Z7xform_xPKfP15HIP_vector_typeIjLj4EE.has_indirect_call, 0

amdhsa.kernels:
  - .agpr_count:     0
    .args:
      - .actual_access:  read_only
        .address_space:  global
        .offset:         0
        .size:           8
        .value_kind:     global_buffer
      - .actual_access:  write_only
        .address_space:  global
        .offset:         8
        .size:           8
        .value_kind:     global_buffer
    .group_segment_fixed_size: 34816
    .kernarg_segment_align: 8
    .kernarg_segment_size: 16
    .language:       OpenCL C
    .language_version:
      - 2
      - 0
    .max_flat_workgroup_size: 256
    .name:           _Z7xform_xPKfP15HIP_vector_typeIjLj4EE
    .private_segment_fixed_size: 0
    .sgpr_count:     37
    .sgpr_spill_count: 0
    .symbol:         _Z7xform_xPKfP15HIP_vector_typeIjLj4EE.kd
    .uniform_work_group_size: 1
    .uses_dynamic_stack: false
    .vgpr_count:     76
    .vgpr_spill_count: 0
    .wavefront_size: 64
  - .agpr_count:     0
    .args:
      - .actual_access:  read_only
        .address_space:  global
        .offset:         0
        .size:           8
        .value_kind:     global_buffer
      - .actual_access:  read_only
        .address_space:  global
        .offset:         8
        .size:           8
        .value_kind:     global_buffer
      - .actual_access:  read_only
        .address_space:  global
        .offset:         16
        .size:           8
        .value_kind:     global_buffer
      - .actual_access:  write_only
        .address_space:  global
        .offset:         24
        .size:           8
        .value_kind:     global_buffer
    .group_segment_fixed_size: 163840
    .kernarg_segment_align: 8
    .kernarg_segment_size: 32
    .language:       OpenCL C
    .language_version:
      - 2
      - 0
    .max_flat_workgroup_size: 512
    .name:           _Z11pwconv_mfmaPKfPK15HIP_vector_typeIjLj4EES0_Pf
    .private_segment_fixed_size: 0
    .sgpr_count:     54
    .sgpr_spill_count: 0
    .symbol:         _Z11pwconv_mfmaPKfPK15HIP_vector_typeIjLj4EES0_Pf.kd
    .uniform_work_group_size: 1
    .uses_dynamic_stack: false
    .vgpr_count:     256
    .vgpr_spill_count: 0
    .wavefront_size: 64
